# MLA tile loop: persistent -m accumulator seed registers as SrcC of the first two QK MFMAs (no per-tile init), DMA sources as 32-bit offsets from ws
# baseline (speedup 1.0000x reference)
; template <int DQ>
; DI AtRd at_rd_init(int lane) {
;     AtRd r; const int kr = lane & 31, h = lane >> 5, i16 = lane & 15, q = i16 >> 2, pp = i16 & 3, blk = (lane >> 4) & 1;
;     const int f = at_kf<DQ>(kr);
;     r.kbase = kr * (DQ * 2) + ((f >> 3) << 7); r.kbase1 = kr * (DQ * 2) + (((f >> 3) ^ 1) << 7);
; #pragma unroll
;     for (int i = 0; i < 4; ++i) r.ko[i] = ((2 * i + h) ^ (f & 7)) << 4;
;     r.vbase = (4 * h + q) * 256 + 8 * pp;
; #pragma unroll
;     for (int t = 0; t < 4; ++t) r.vo[t] = ((2 * t + blk) ^ ((4 * h + q) & 7)) << 5;
;     return r;
; template <int DQ>
; DI AtDma at_dma_init(int ld_bytes, int wave, int lane) {
;     AtDma d; d.rope = 0u;
;     constexpr int PPR = DQ / 8;
; #pragma unroll
;     for (int k = 0; k < DQ / 64; ++k) { const int L = (wave + 8 * k) * 64 + lane, r = L / PPR, pc = (L % PPR) ^ at_kf<DQ>(r);
;         if (DQ == 192 && pc >= 16) { d.ko[k] = (unsigned)(r * 128 + (pc - 16) * 16); d.rope |= 1u << k; } else d.ko[k] = (unsigned)(r * ld_bytes + pc * 16); }
;     if (DQ == 128) d.ko[2] = 0u;
; #pragma unroll
;     for (int k = 0; k < 2; ++k) { const int L = (wave + 8 * k) * 64 + lane, r = L >> 4, pc = (L & 15) ^ (2 * (r & 7)); d.vo[k] = (unsigned)(r * ld_bytes + pc * 16); }
;     return d;
; }
.LBB0_530:
	s_cmp_gt_i32 s24, 5
	s_cselect_b64 s[0:1], -1, 0
	s_cmp_lt_i32 s25, 6
	s_cselect_b64 s[2:3], -1, 0
	s_or_b64 s[0:1], s[0:1], s[2:3]
	s_and_b64 vcc, exec, s[0:1]
	s_cbranch_vccnz .LBB0_622
	s_bitcmp1_b32 s26, 1
	s_cbranch_scc1 .LBB0_560
	v_readfirstlane_b32 s2, v0
	s_movk_i32 s0, 0xffc0
	s_nop 0
	v_mov_b32_e32 v1, s2
	v_bfi_b32 v2, s0, v1, v0
	s_mov_b32 s0, 0x2aaaaaab
	v_mul_hi_i32 v1, v2, s0
	v_lshrrev_b32_e32 v3, 31, v1
	v_ashrrev_i32_e32 v1, 2, v1
	v_add_u32_e32 v1, v1, v3
	v_mul_lo_u32 v3, v1, 24
	v_sub_u32_e32 v3, v2, v3
	v_lshrrev_b32_e32 v4, 1, v1
	v_bitop3_b32 v3, v4, v3, 7 bitop3:0x6c
	v_cmp_gt_i32_e32 vcc, 16, v3
	v_lshlrev_b32_e32 v3, 4, v3
	s_and_saveexec_b64 s[0:1], vcc
	s_xor_b64 s[0:1], exec, s[0:1]
	v_lshl_add_u32 v162, v1, 12, v3
	s_or_saveexec_b64 s[0:1], s[0:1]
	v_mov_b32_e32 v4, 0
	s_xor_b64 exec, exec, s[0:1]
	v_lshlrev_b32_e32 v1, 7, v1
	s_movk_i32 s3, 0xff00
	v_add3_u32 v162, v1, v3, s3
	v_mov_b32_e32 v4, 1
	s_or_b64 exec, exec, s[0:1]
	v_add_u32_e32 v5, 0x200, v2
	s_mov_b32 s0, 0x2aaaaaab
	v_mul_hi_i32 v1, v5, s0
	v_lshrrev_b32_e32 v3, 31, v1
	v_ashrrev_i32_e32 v1, 2, v1
	v_add_u32_e32 v1, v1, v3
	v_mul_lo_u32 v3, v1, 24
	v_sub_u32_e32 v3, v5, v3
	v_lshrrev_b32_e32 v6, 1, v1
	v_bitop3_b32 v3, v6, v3, 7 bitop3:0x6c
	v_cmp_gt_i32_e32 vcc, 16, v3
	v_lshlrev_b32_e32 v3, 4, v3
	s_and_saveexec_b64 s[0:1], vcc
	s_xor_b64 s[0:1], exec, s[0:1]
	v_lshl_add_u32 v164, v1, 12, v3
	s_andn2_saveexec_b64 s[0:1], s[0:1]
	v_lshlrev_b32_e32 v1, 7, v1
	s_movk_i32 s3, 0xff00
	v_add3_u32 v164, v1, v3, s3
	v_or_b32_e32 v4, 2, v4
	s_or_b64 exec, exec, s[0:1]
	v_add_u32_e32 v3, 0x400, v2
	s_mov_b32 s0, 0x2aaaaaab
	v_mul_hi_i32 v1, v3, s0
	v_lshrrev_b32_e32 v6, 31, v1
	v_ashrrev_i32_e32 v1, 2, v1
	v_add_u32_e32 v1, v1, v6
	v_mul_lo_u32 v6, v1, 24
	v_sub_u32_e32 v3, v3, v6
	v_lshrrev_b32_e32 v6, 1, v1
	v_bitop3_b32 v3, v6, v3, 7 bitop3:0x6c
	v_cmp_gt_i32_e32 vcc, 16, v3
	v_lshlrev_b32_e32 v6, 4, v3
	s_and_saveexec_b64 s[0:1], vcc
	s_xor_b64 s[0:1], exec, s[0:1]
	v_lshl_add_u32 v166, v1, 12, v6
	s_or_saveexec_b64 s[0:1], s[0:1]
	v_and_b32_e32 v3, 63, v0
	s_xor_b64 exec, exec, s[0:1]
	v_lshlrev_b32_e32 v1, 7, v1
	s_movk_i32 s3, 0xff00
	v_add3_u32 v166, v1, v6, s3
	v_or_b32_e32 v4, 4, v4
	s_or_b64 exec, exec, s[0:1]
	v_lshrrev_b32_e32 v6, 5, v3
	v_bfe_u32 v10, v0, 1, 3
	s_lshr_b32 s2, s2, 6
	v_bitop3_b32 v11, v6, v10, 2 bitop3:0x36
	s_add_u32 s0, s50, 0x2c5ae000
	v_lshrrev_b32_e32 v1, 1, v0
	v_lshlrev_b32_e32 v180, 4, v11
	v_bitop3_b32 v11, v6, v10, 4 bitop3:0x36
	v_bitop3_b32 v10, v6, v10, 6 bitop3:0x36
	s_addc_u32 s1, s51, 0
	v_bitop3_b32 v1, v6, v1, 7 bitop3:0x78
	v_lshlrev_b32_e32 v182, 4, v10
	v_bfe_u32 v10, v3, 2, 2
	v_lshlrev_b32_e32 v6, 2, v6
	s_add_u32 s8, s50, 0x304ae000
	v_lshrrev_b32_e32 v8, 2, v3
	v_lshrrev_b32_e32 v9, 4, v3
	v_lshlrev_b32_e32 v181, 4, v11
	v_bfe_u32 v3, v3, 4, 1
	v_or_b32_e32 v11, v6, v10
	s_addc_u32 s9, s51, 0
	v_bitop3_b32 v14, v6, v3, v10 bitop3:0x36
	v_bitop3_b32 v3, v3, v11, 4 bitop3:0x36
	s_lshr_b32 s4, s23, 31
	v_and_b32_e32 v7, 31, v0
	v_lshlrev_b32_e32 v183, 5, v14
	v_or_b32_e32 v14, 2, v9
	v_lshlrev_b32_e32 v185, 5, v3
	v_or_b32_e32 v3, 6, v9
	s_movk_i32 s3, 0x180
	s_add_i32 s4, s23, s4
	v_ashrrev_i32_e32 v2, 4, v2
	v_bitop3_b32 v14, v6, v14, v10 bitop3:0x36
	v_bitop3_b32 v3, v6, v3, v10 bitop3:0x36
	v_and_b32_e32 v9, 15, v0
	v_mad_u32_u24 v187, v7, s3, 0
	s_add_i32 s3, s23, s22
	s_ashr_i32 s4, s4, 1
	v_lshlrev_b32_e32 v10, 1, v2
	s_sub_i32 s10, s3, s4
	v_bitop3_b32 v10, v10, v9, 14 bitop3:0x6c
	v_lshlrev_b32_e32 v2, 12, v2
	s_add_u32 s12, s50, 0x2e0ae000
	v_lshl_or_b32 v168, v10, 4, v2
	v_ashrrev_i32_e32 v2, 4, v5
	s_addc_u32 s13, s51, 0
	v_lshlrev_b32_e32 v5, 1, v2
	s_add_u32 s14, s50, 0x2c48e000
	v_bitop3_b32 v5, v5, v9, 14 bitop3:0x6c
	v_lshlrev_b32_e32 v2, 12, v2
	s_addc_u32 s15, s51, 0
	v_lshl_or_b32 v170, v5, 4, v2
	v_lshl_or_b32 v189, s2, 5, v7
	s_lshl_b32 s2, s2, 10
	v_and_b32_e32 v2, 1, v4
	s_add_i32 s27, s2, 0
	v_cmp_eq_u32_e64 s[2:3], 0, v2
	v_and_b32_e32 v2, 2, v4
	s_abs_i32 s16, s23
	v_cmp_eq_u32_e64 s[4:5], 0, v2
	v_cvt_f32_u32_e32 v2, s16
	s_sub_i32 s18, 0, s16
	s_ashr_i32 s17, s10, 31
	s_abs_i32 s10, s10
	v_rcp_iflag_f32_e32 v2, v2
	v_lshlrev_b32_e32 v13, 3, v0
	v_lshlrev_b32_e32 v186, 5, v3
	v_lshrrev_b32_e32 v3, 2, v0
	v_mul_f32_e32 v2, 0x4f7ffffe, v2
	v_cvt_u32_f32_e32 v2, v2
	v_lshlrev_b32_e32 v12, 8, v11
	v_and_b32_e32 v13, 24, v13
	v_and_b32_e32 v6, 8, v3
	v_readfirstlane_b32 s19, v2
	s_mul_i32 s18, s18, s19
	s_mul_hi_u32 s18, s19, s18
	s_add_i32 s19, s19, s18
	s_mul_hi_u32 s18, s10, s19
	s_mul_i32 s18, s18, s16
	s_sub_i32 s10, s10, s18
	s_sub_i32 s18, s10, s16
	s_cmp_ge_u32 s10, s16
	s_cselect_b32 s10, s18, s10
	s_sub_i32 s18, s10, s16
	s_cmp_ge_u32 s10, s16
	s_cselect_b32 s10, s18, s10
	s_xor_b32 s10, s10, s17
	v_mov_b32_e32 v3, 0
	v_and_b32_e32 v8, 8, v8
	v_and_b32_e32 v4, 4, v4
	s_sub_i32 s34, s10, s17
	v_mbcnt_lo_u32_b32 v2, -1, 0
	v_lshlrev_b32_e32 v1, 4, v1
	v_lshlrev_b32_e32 v184, 5, v14
	s_mov_b32 s11, 0
	v_add3_u32 v188, 0, v12, v13
	v_add_u32_e32 v190, 0x400, v189
	v_mov_b32_e32 v163, v3
	v_mov_b32_e32 v165, v3
	v_cmp_eq_u32_e64 s[6:7], 0, v4
	v_mov_b32_e32 v167, v3
	v_mov_b32_e32 v169, v3
	v_mov_b32_e32 v171, v3
	s_addk_i32 s34, 0x100
	s_mov_b64 s[16:17], -1
	s_movk_i32 s35, 0xc00
	v_lshlrev_b32_e32 v172, 1, v6
	s_add_i32 s40, s27, 0x2000
	s_add_i32 s41, s27, 0x4000
	s_mov_b64 s[18:19], 0x100
	s_add_i32 s54, s27, 0x12000
	s_add_i32 s55, s27, 0x14000
	s_mov_b32 s58, 0x41000000
	v_lshlrev_b32_e32 v174, 1, v8
	v_mbcnt_hi_u32_b32 v191, -1, v2
	v_mov_b32_e32 v248, 0x2000
	v_mov_b32_e32 v249, 0x40000
	v_cndmask_b32_e64 v221, v248, v249, s[2:3]
	v_cndmask_b32_e64 v223, v248, v249, s[4:5]
	v_cndmask_b32_e64 v250, v248, v249, s[6:7]
	v_add_u32_e32 v240, v187, v1
	v_add_u32_e32 v241, v187, v180
	v_add_u32_e32 v242, v187, v181
	v_add_u32_e32 v243, v187, v182
	v_add_u32_e32 v244, 0x12000, v188
	v_add_u32_e32 v245, v244, v184
	v_add_u32_e32 v246, v244, v185
	v_add_u32_e32 v247, v244, v186
	v_add_u32_e32 v244, v244, v183
	s_branch .LBB0_546

;     DI const char* kb(int j) const { return KV + (size_t)keyrow0(j) * 4096 + head * 512; }
;     DI const char* vb(int j) const { return KV + (size_t)keyrow0(j) * 4096 + head * 512 + 256; }
;     DI const char* rb(int j) const { return KR + (size_t)keyrow0(j) * 128; }
;     DI const char* kb(int q) const { return Z + (size_t)keyrow0(q) * (L1IN * 2) + (1024 + kvh * 128) * 2; }
;     DI const char* vb(int q) const { return Z + (size_t)keyrow0(q) * (L1IN * 2) + (1280 + kvh * 128) * 2; }
;     DI const char* kb(int j) const { return Z + (size_t)keyrow0(j) * (L1IN * 2) + (2560 + head * 128) * 2; }
;     DI const char* vb(int j) const { return Z + (size_t)keyrow0(j) * (L1IN * 2) + (3584 + head * 128) * 2; }
; template <int DQ, class Drv>
; DI void at_run3(LAS unsigned char* lds, const Drv& D, const int n, const AtRd& rd, const AtDma& dm, const bf16x8 (&qf)[DQ / 16], f32x16 (&o)[4], float& m, float& l, const float c2, const int lane, const int wave) {
;     __syncthreads();
;     at_dma_k<DQ>(lds, D.kb(0), D.rb(0), dm, wave); at_dma_v(lds + AT_KSLOT, D.vb(0), dm, wave);
;     if (n > 1) { at_dma_k<DQ>(lds + AT4_SLOT, D.kb(1), D.rb(1), dm, wave); at_dma_v(lds + AT4_SLOT + AT_KSLOT, D.vb(1), dm, wave);
;         if (DQ == 192) asm volatile("s_waitcnt vmcnt(5)" ::: "memory"); else asm volatile("s_waitcnt vmcnt(4)" ::: "memory"); }
;     else asm volatile("s_waitcnt vmcnt(0)" ::: "memory");
;     __syncthreads();
; DI void phase_attn0(const Params& p, LAS unsigned char* lds, int G, int bid) {
;     ...
;         bf16x8 qf[12];
; #pragma unroll
;         for (int s = 0; s < 12; ++s) qf[s] = *(const bf16x8*)(Q0 + (size_t)qrow * 1536 + T.head * 192 + 16 * s + 8 * h);
;         f32x16 o[4];
; #pragma unroll
;         for (int t = 0; t < 4; ++t)
; #pragma unroll
;             for (int i = 0; i < 16; ++i) o[t][i] = 0.f;
;         float m = AT_M0, l = 0.f;
.LBB0_554:
	s_and_b32 s67, s10, 7
	v_mov_b64_e32 v[4:5], s[0:1]
	v_mad_i64_i32 v[4:5], s[30:31], v176, s35, v[4:5]
	s_mul_i32 s10, s67, 0x180
	v_lshl_add_u64 v[4:5], v[4:5], 0, s[10:11]
	v_mov_b32_e32 v173, v3
	v_lshl_add_u64 v[4:5], v[4:5], 0, v[172:173]
	v_ashrrev_i32_e32 v179, 31, v178
	global_load_dwordx4 v[158:161], v[4:5], off
	global_load_dwordx4 v[154:157], v[4:5], off offset:32
	global_load_dwordx4 v[150:153], v[4:5], off offset:64
	global_load_dwordx4 v[146:149], v[4:5], off offset:96
	global_load_dwordx4 v[142:145], v[4:5], off offset:128
	global_load_dwordx4 v[138:141], v[4:5], off offset:160
	global_load_dwordx4 v[134:137], v[4:5], off offset:192
	global_load_dwordx4 v[130:133], v[4:5], off offset:224
	global_load_dwordx4 v[126:129], v[4:5], off offset:256
	global_load_dwordx4 v[122:125], v[4:5], off offset:288
	global_load_dwordx4 v[118:121], v[4:5], off offset:320
	global_load_dwordx4 v[114:117], v[4:5], off offset:352
	v_lshlrev_b64 v[4:5], 12, v[178:179]
	v_lshl_add_u64 v[4:5], s[12:13], 0, v[4:5]
	s_lshl_b32 s10, s67, 9
	v_lshlrev_b64 v[6:7], 7, v[178:179]
	v_lshl_add_u64 v[4:5], v[4:5], 0, s[10:11]
	v_lshl_add_u64 v[6:7], s[14:15], 0, v[6:7]
	v_cndmask_b32_e64 v9, v7, v5, s[2:3]
	v_cndmask_b32_e64 v8, v6, v4, s[2:3]
	s_mov_b32 m0, s27
	v_lshl_add_u64 v[8:9], v[8:9], 0, v[162:163]
	s_waitcnt vmcnt(0)
	s_barrier
	global_load_lds_dwordx4 v[8:9], off
	v_cndmask_b32_e64 v9, v7, v5, s[4:5]
	v_cndmask_b32_e64 v8, v6, v4, s[4:5]
	v_lshl_add_u64 v[8:9], v[8:9], 0, v[164:165]
	s_mov_b32 m0, s40
	v_cndmask_b32_e64 v7, v7, v5, s[6:7]
	v_cndmask_b32_e64 v6, v6, v4, s[6:7]
	global_load_lds_dwordx4 v[8:9], off
	v_lshl_add_u64 v[6:7], v[6:7], 0, v[166:167]
	s_mov_b32 m0, s41
	v_mov_b32_e32 v16, v3
	global_load_lds_dwordx4 v[6:7], off
	v_lshl_add_u64 v[6:7], v[4:5], 0, v[168:169]
	v_lshl_add_u64 v[6:7], v[6:7], 0, s[18:19]
	s_mov_b32 m0, s54
	v_lshl_add_u64 v[4:5], v[4:5], 0, v[170:171]
	global_load_lds_dwordx4 v[6:7], off
	v_lshl_add_u64 v[4:5], v[4:5], 0, s[18:19]
	s_mov_b32 m0, s55
	v_mov_b32_e32 v17, v3
	global_load_lds_dwordx4 v[4:5], off
	s_add_u32 s100, s12, s10
	s_addc_u32 s101, s13, 0
	v_add_u32_e32 v4, 64, v178
	v_ashrrev_i32_e32 v5, 31, v4
	v_lshlrev_b64 v[6:7], 12, v[4:5]
	v_lshlrev_b64 v[4:5], 7, v[4:5]
	v_lshl_add_u64 v[6:7], s[100:101], 0, v[6:7]
	v_lshl_add_u64 v[4:5], s[14:15], 0, v[4:5]
	v_cndmask_b32_e64 v9, v5, v7, s[2:3]
	v_cndmask_b32_e64 v8, v4, v6, s[2:3]
	v_lshl_add_u64 v[8:9], v[8:9], 0, v[162:163]
	s_add_i32 m0, s27, 0x6000
	s_nop 0
	global_load_lds_dwordx4 v[8:9], off
	v_cndmask_b32_e64 v9, v5, v7, s[4:5]
	v_cndmask_b32_e64 v8, v4, v6, s[4:5]
	v_lshl_add_u64 v[8:9], v[8:9], 0, v[164:165]
	s_add_i32 m0, s27, 0x8000
	v_cndmask_b32_e64 v5, v5, v7, s[6:7]
	v_cndmask_b32_e64 v4, v4, v6, s[6:7]
	global_load_lds_dwordx4 v[8:9], off
	v_lshl_add_u64 v[4:5], v[4:5], 0, v[166:167]
	s_add_i32 m0, s27, 0xa000
	s_nop 0
	global_load_lds_dwordx4 v[4:5], off
	v_lshl_add_u64 v[4:5], v[6:7], 0, v[168:169]
	s_add_i32 m0, s27, 0x16000
	v_lshl_add_u64 v[4:5], v[4:5], 0, s[18:19]
	global_load_lds_dwordx4 v[4:5], off
	v_lshl_add_u64 v[4:5], v[6:7], 0, v[170:171]
	s_add_i32 m0, s27, 0x18000
	v_lshl_add_u64 v[4:5], v[4:5], 0, s[18:19]
	global_load_lds_dwordx4 v[4:5], off
	s_mov_b32 s98, 0
	s_mov_b32 s99, 2
	s_waitcnt vmcnt(5)
	v_or_b32_e32 v175, 0x300, v2
	s_add_u32 s30, s12, s10
	v_mov_b32_e32 v2, v3
	v_mov_b32_e32 v4, v3
	v_mov_b32_e32 v5, v3
	v_mov_b32_e32 v6, v3
	v_mov_b32_e32 v7, v3
	v_mov_b32_e32 v8, v3
	v_mov_b32_e32 v9, v3
	v_mov_b32_e32 v10, v3
	v_mov_b32_e32 v11, v3
	v_mov_b32_e32 v12, v3
	v_mov_b32_e32 v13, v3
	v_mov_b32_e32 v14, v3
	v_mov_b32_e32 v15, v3
	v_mov_b64_e32 v[32:33], v[16:17]
	v_mov_b64_e32 v[48:49], v[16:17]
	v_mov_b64_e32 v[64:65], v[16:17]
	v_mov_b64_e32 v[80:81], v[16:17]
	v_ashrrev_i32_e32 v177, 31, v176
	s_addc_u32 s31, s13, 0
	s_add_i32 s10, s68, 1
	s_mov_b32 s68, 0
	v_mov_b32_e32 v173, 0
	v_mov_b32_e32 v179, 0xc1f00000
	v_xor_b32_e32 v224, 0x80000000, v179
	v_mov_b32_e32 v225, v224
	v_mov_b64_e32 v[226:227], v[224:225]
	v_mov_b64_e32 v[228:229], v[224:225]
	v_mov_b64_e32 v[230:231], v[224:225]
	v_mov_b64_e32 v[232:233], v[224:225]
	v_mov_b64_e32 v[234:235], v[224:225]
	v_mov_b64_e32 v[236:237], v[224:225]
	v_mov_b64_e32 v[238:239], v[224:225]
	s_mov_b32 s69, 64
	v_mov_b64_e32 v[30:31], v[14:15]
	v_mov_b64_e32 v[28:29], v[12:13]
	v_mov_b64_e32 v[26:27], v[10:11]
	v_mov_b64_e32 v[24:25], v[8:9]
	v_mov_b64_e32 v[22:23], v[6:7]
	v_mov_b64_e32 v[20:21], v[4:5]
	v_mov_b64_e32 v[18:19], v[2:3]
	v_mov_b64_e32 v[46:47], v[14:15]
	v_mov_b64_e32 v[44:45], v[12:13]
	v_mov_b64_e32 v[42:43], v[10:11]
	v_mov_b64_e32 v[40:41], v[8:9]
	v_mov_b64_e32 v[38:39], v[6:7]
	v_mov_b64_e32 v[36:37], v[4:5]
	v_mov_b64_e32 v[34:35], v[2:3]
	v_mov_b64_e32 v[62:63], v[14:15]
	v_mov_b64_e32 v[60:61], v[12:13]
	v_mov_b64_e32 v[58:59], v[10:11]
	v_mov_b64_e32 v[56:57], v[8:9]
	v_mov_b64_e32 v[54:55], v[6:7]
	v_mov_b64_e32 v[52:53], v[4:5]
	v_mov_b64_e32 v[50:51], v[2:3]
	v_mov_b64_e32 v[78:79], v[14:15]
	v_mov_b64_e32 v[76:77], v[12:13]
	v_mov_b64_e32 v[74:75], v[10:11]
	v_mov_b64_e32 v[72:73], v[8:9]
	v_mov_b64_e32 v[70:71], v[6:7]
	v_mov_b64_e32 v[68:69], v[4:5]
	v_mov_b64_e32 v[66:67], v[2:3]
	s_waitcnt vmcnt(5) lgkmcnt(0)
	s_barrier
	s_branch .LBB0_556

; #define LAS __attribute__((address_space(3)))
; #define MFMA32(a, b, c) __builtin_amdgcn_mfma_f32_32x32x16_bf16((a), (b), (c), 0, 0, 0)
;     DI const char* kb(int j) const { return KV + (size_t)keyrow0(j) * 4096 + head * 512; }
;     DI const char* vb(int j) const { return KV + (size_t)keyrow0(j) * 4096 + head * 512 + 256; }
;     DI const char* rb(int j) const { return KR + (size_t)keyrow0(j) * 128; }
;     DI const char* kb(int q) const { return Z + (size_t)keyrow0(q) * (L1IN * 2) + (1024 + kvh * 128) * 2; }
;     DI const char* vb(int q) const { return Z + (size_t)keyrow0(q) * (L1IN * 2) + (1280 + kvh * 128) * 2; }
;     DI const char* kb(int j) const { return Z + (size_t)keyrow0(j) * (L1IN * 2) + (2560 + head * 128) * 2; }
;     DI const char* vb(int j) const { return Z + (size_t)keyrow0(j) * (L1IN * 2) + (3584 + head * 128) * 2; }
; #pragma unroll
;     for (int i = 0; i < 16; ++i) { s0[i] = init; s1[i] = init; }
;     const LAS unsigned char* kp0 = ks + rd.kbase; const LAS unsigned char* kp1 = ks + rd.kbase1;
; #pragma unroll
;     for (int s = 0; s < DQ / 16; ++s) {
;         const LAS unsigned char* kp = (DQ == 128) ? ((s >> 2) ? kp1 : kp0) : kp0 + ((s >> 2) << 7);
;         const bf16x8 a0 = *(const LAS bf16x8*)(kp + rd.ko[s & 3]);
;         const bf16x8 a1 = *(const LAS bf16x8*)(kp + 32 * (DQ * 2) + rd.ko[s & 3]);
;         s0 = MFMA32(a0, qf[s], s0); s1 = MFMA32(a1, qf[s], s1);
;     }
; }
; template <int DQ, class Drv>
; DI void at_run3(LAS unsigned char* lds, const Drv& D, const int n, const AtRd& rd, const AtDma& dm, const bf16x8 (&qf)[DQ / 16], f32x16 (&o)[4], float& m, float& l, const float c2, const int lane, const int wave) {
;     ...
;     for (int j = 0; j < n; ++j) {
;         const int nx2 = cur == 0 ? 2 : cur - 1;
;         if (j + 2 < n) { at_dma_k<DQ>(lds + nx2 * AT4_SLOT, D.kb(j + 2), D.rb(j + 2), dm, wave); at_dma_v(lds + nx2 * AT4_SLOT + AT_KSLOT, D.vb(j + 2), dm, wave); }
;         if (D.act(j)) {
;             f32x16 a0, a1;
;             at_qk<DQ>(lds + cur * AT4_SLOT, rd, qf, a0, a1);
.LBB0_556:
	s_mov_b32 s70, s98
	s_mov_b32 s71, s99
	s_add_i32 s98, s98, 1
	s_cmp_eq_u32 s98, 3
	s_cselect_b32 s98, 0, s98
	s_add_i32 s99, s99, 1
	s_cmp_eq_u32 s99, 3
	s_cselect_b32 s99, 0, s99
	s_add_i32 s100, s68, 2
	s_cmp_gt_u32 s100, s10
	s_cbranch_scc1 .Lmla_nodma
	s_mul_i32 s72, s71, 0x6000
	s_add_i32 s72, s27, s72
	s_lshl_b32 s71, s71, 14
	s_add_i32 s71, s27, s71
	s_cmp_eq_u32 s68, 0
	s_cbranch_scc1 .Lmla_dma_full
	s_cmp_eq_u32 s68, 2
	s_cbranch_scc1 .Lmla_dma_full
	v_add_u32_e32 v216, v216, v221
	v_add_u32_e32 v217, v217, v223
	v_add_u32_e32 v218, v218, v250
	v_add_u32_e32 v219, 0x40000, v219
	v_add_u32_e32 v220, 0x40000, v220
	s_branch .Lmla_dma_issue
.Lmla_dma_full:
	s_add_i32 s100, s69, 64
	s_cmp_lt_u32 s68, 2
	s_cselect_b64 vcc, -1, 0
	v_cndmask_b32_e32 v2, v175, v178, vcc
	v_add_u32_e32 v4, s100, v2
	v_ashrrev_i32_e32 v5, 31, v4
	v_lshlrev_b64 v[6:7], 12, v[4:5]
	v_lshlrev_b64 v[4:5], 7, v[4:5]
	v_lshl_add_u64 v[6:7], s[30:31], 0, v[6:7]
	v_lshl_add_u64 v[4:5], s[14:15], 0, v[4:5]
	v_cndmask_b32_e64 v216, v4, v6, s[2:3]
	v_cndmask_b32_e64 v217, v4, v6, s[4:5]
	v_cndmask_b32_e64 v218, v4, v6, s[6:7]
	v_add_u32_e32 v216, v216, v162
	v_add_u32_e32 v217, v217, v164
	v_add_u32_e32 v218, v218, v166
	v_add_u32_e32 v219, v6, v168
	v_add_u32_e32 v220, v6, v170
	s_sub_u32 s100, 0x100, s50
	v_subrev_u32_e32 v216, s50, v216
	v_subrev_u32_e32 v217, s50, v217
	v_subrev_u32_e32 v218, s50, v218
	v_add_u32_e32 v219, s100, v219
	v_add_u32_e32 v220, s100, v220
.Lmla_dma_issue:
	s_mov_b32 m0, s72
	s_nop 0
	global_load_lds_dwordx4 v216, s[50:51]
	s_add_i32 m0, s72, 0x2000
	s_nop 0
	global_load_lds_dwordx4 v217, s[50:51]
	s_add_i32 m0, s72, 0x4000
	s_nop 0
	global_load_lds_dwordx4 v218, s[50:51]
	s_add_i32 m0, s71, 0x12000
	s_nop 0
	global_load_lds_dwordx4 v219, s[50:51]
	s_add_i32 m0, s71, 0x14000
	s_nop 0
	global_load_lds_dwordx4 v220, s[50:51]
.Lmla_nodma:
	s_cmp_eq_u32 s70, 1
	s_cbranch_scc1 .Lmla_qk1
	s_cmp_eq_u32 s70, 2
	s_cbranch_scc1 .Lmla_qk2
	ds_read_b128 v[4:7], v240
	ds_read_b128 v[8:11], v240 offset:128
	s_waitcnt lgkmcnt(0)
	v_mfma_f32_32x32x16_bf16 v[98:113], v[4:7], v[158:161], v[224:239]
	ds_read_b128 v[4:7], v240 offset:12288
	ds_read_b128 v[12:15], v240 offset:256
	s_waitcnt lgkmcnt(0)
	v_mfma_f32_32x32x16_bf16 v[82:97], v[4:7], v[158:161], v[224:239]
	ds_read_b128 v[4:7], v241
	ds_read_b128 v[192:195], v241 offset:128
	s_waitcnt lgkmcnt(0)
	v_mfma_f32_32x32x16_bf16 v[98:113], v[4:7], v[154:157], v[98:113]
	ds_read_b128 v[4:7], v241 offset:12288
	ds_read_b128 v[196:199], v241 offset:256
	s_waitcnt lgkmcnt(0)
	v_mfma_f32_32x32x16_bf16 v[82:97], v[4:7], v[154:157], v[82:97]
	ds_read_b128 v[4:7], v242
	ds_read_b128 v[200:203], v242 offset:128
	s_waitcnt lgkmcnt(0)
	v_mfma_f32_32x32x16_bf16 v[98:113], v[4:7], v[150:153], v[98:113]
	ds_read_b128 v[4:7], v242 offset:12288
	ds_read_b128 v[204:207], v242 offset:256
	s_waitcnt lgkmcnt(0)
	v_mfma_f32_32x32x16_bf16 v[82:97], v[4:7], v[150:153], v[82:97]
	ds_read_b128 v[4:7], v243
	ds_read_b128 v[208:211], v243 offset:128
	s_waitcnt lgkmcnt(0)
	v_mfma_f32_32x32x16_bf16 v[98:113], v[4:7], v[146:149], v[98:113]
	ds_read_b128 v[4:7], v243 offset:12288
	ds_read_b128 v[212:215], v243 offset:256
	s_waitcnt lgkmcnt(0)
	v_mfma_f32_32x32x16_bf16 v[82:97], v[4:7], v[146:149], v[82:97]
	v_mfma_f32_32x32x16_bf16 v[98:113], v[8:11], v[142:145], v[98:113]
	ds_read_b128 v[4:7], v240 offset:12416
	ds_read_b128 v[8:11], v240 offset:12544
	s_waitcnt lgkmcnt(0)
	v_mfma_f32_32x32x16_bf16 v[82:97], v[4:7], v[142:145], v[82:97]
	v_mfma_f32_32x32x16_bf16 v[98:113], v[192:195], v[138:141], v[98:113]
	ds_read_b128 v[4:7], v241 offset:12416
	ds_read_b128 v[192:195], v241 offset:12544
	s_waitcnt lgkmcnt(0)
	v_mfma_f32_32x32x16_bf16 v[82:97], v[4:7], v[138:141], v[82:97]
	v_mfma_f32_32x32x16_bf16 v[98:113], v[200:203], v[134:137], v[98:113]
	ds_read_b128 v[4:7], v242 offset:12416
	ds_read_b128 v[200:203], v242 offset:12544
	s_waitcnt lgkmcnt(0)
	v_mfma_f32_32x32x16_bf16 v[82:97], v[4:7], v[134:137], v[82:97]
	v_mfma_f32_32x32x16_bf16 v[98:113], v[208:211], v[130:133], v[98:113]
	ds_read_b128 v[4:7], v243 offset:12416
	ds_read_b128 v[208:211], v243 offset:12544
	s_waitcnt lgkmcnt(0)
	v_mfma_f32_32x32x16_bf16 v[82:97], v[4:7], v[130:133], v[82:97]
	v_mfma_f32_32x32x16_bf16 v[98:113], v[12:15], v[126:129], v[98:113]
	v_mfma_f32_32x32x16_bf16 v[82:97], v[8:11], v[126:129], v[82:97]
	v_mfma_f32_32x32x16_bf16 v[98:113], v[196:199], v[122:125], v[98:113]
	v_mfma_f32_32x32x16_bf16 v[82:97], v[192:195], v[122:125], v[82:97]
	v_mfma_f32_32x32x16_bf16 v[98:113], v[204:207], v[118:121], v[98:113]
	v_mfma_f32_32x32x16_bf16 v[82:97], v[200:203], v[118:121], v[82:97]
	v_mfma_f32_32x32x16_bf16 v[98:113], v[212:215], v[114:117], v[98:113]
	v_mfma_f32_32x32x16_bf16 v[82:97], v[208:211], v[114:117], v[82:97]
	s_branch .Lmla_qkd
; #define LAS __attribute__((address_space(3)))
; #define MFMA32(a, b, c) __builtin_amdgcn_mfma_f32_32x32x16_bf16((a), (b), (c), 0, 0, 0)
; #pragma unroll
;     for (int i = 0; i < 16; ++i) { s0[i] = init; s1[i] = init; }
;     const LAS unsigned char* kp0 = ks + rd.kbase; const LAS unsigned char* kp1 = ks + rd.kbase1;
; #pragma unroll
;     for (int s = 0; s < DQ / 16; ++s) {
;         const LAS unsigned char* kp = (DQ == 128) ? ((s >> 2) ? kp1 : kp0) : kp0 + ((s >> 2) << 7);
;         const bf16x8 a0 = *(const LAS bf16x8*)(kp + rd.ko[s & 3]);
;         const bf16x8 a1 = *(const LAS bf16x8*)(kp + 32 * (DQ * 2) + rd.ko[s & 3]);
;         s0 = MFMA32(a0, qf[s], s0); s1 = MFMA32(a1, qf[s], s1);
;     }
; }
.Lmla_qk1:
	ds_read_b128 v[4:7], v240 offset:24576
	ds_read_b128 v[8:11], v240 offset:24704
	s_waitcnt lgkmcnt(0)
	v_mfma_f32_32x32x16_bf16 v[98:113], v[4:7], v[158:161], v[224:239]
	ds_read_b128 v[4:7], v240 offset:36864
	ds_read_b128 v[12:15], v240 offset:24832
	s_waitcnt lgkmcnt(0)
	v_mfma_f32_32x32x16_bf16 v[82:97], v[4:7], v[158:161], v[224:239]
	ds_read_b128 v[4:7], v241 offset:24576
	ds_read_b128 v[192:195], v241 offset:24704
	s_waitcnt lgkmcnt(0)
	v_mfma_f32_32x32x16_bf16 v[98:113], v[4:7], v[154:157], v[98:113]
	ds_read_b128 v[4:7], v241 offset:36864
	ds_read_b128 v[196:199], v241 offset:24832
	s_waitcnt lgkmcnt(0)
	v_mfma_f32_32x32x16_bf16 v[82:97], v[4:7], v[154:157], v[82:97]
	ds_read_b128 v[4:7], v242 offset:24576
	ds_read_b128 v[200:203], v242 offset:24704
	s_waitcnt lgkmcnt(0)
	v_mfma_f32_32x32x16_bf16 v[98:113], v[4:7], v[150:153], v[98:113]
	ds_read_b128 v[4:7], v242 offset:36864
	ds_read_b128 v[204:207], v242 offset:24832
	s_waitcnt lgkmcnt(0)
	v_mfma_f32_32x32x16_bf16 v[82:97], v[4:7], v[150:153], v[82:97]
	ds_read_b128 v[4:7], v243 offset:24576
	ds_read_b128 v[208:211], v243 offset:24704
	s_waitcnt lgkmcnt(0)
	v_mfma_f32_32x32x16_bf16 v[98:113], v[4:7], v[146:149], v[98:113]
	ds_read_b128 v[4:7], v243 offset:36864
	ds_read_b128 v[212:215], v243 offset:24832
	s_waitcnt lgkmcnt(0)
	v_mfma_f32_32x32x16_bf16 v[82:97], v[4:7], v[146:149], v[82:97]
	v_mfma_f32_32x32x16_bf16 v[98:113], v[8:11], v[142:145], v[98:113]
	ds_read_b128 v[4:7], v240 offset:36992
	ds_read_b128 v[8:11], v240 offset:37120
	s_waitcnt lgkmcnt(0)
	v_mfma_f32_32x32x16_bf16 v[82:97], v[4:7], v[142:145], v[82:97]
	v_mfma_f32_32x32x16_bf16 v[98:113], v[192:195], v[138:141], v[98:113]
	ds_read_b128 v[4:7], v241 offset:36992
	ds_read_b128 v[192:195], v241 offset:37120
	s_waitcnt lgkmcnt(0)
	v_mfma_f32_32x32x16_bf16 v[82:97], v[4:7], v[138:141], v[82:97]
	v_mfma_f32_32x32x16_bf16 v[98:113], v[200:203], v[134:137], v[98:113]
	ds_read_b128 v[4:7], v242 offset:36992
	ds_read_b128 v[200:203], v242 offset:37120
	s_waitcnt lgkmcnt(0)
	v_mfma_f32_32x32x16_bf16 v[82:97], v[4:7], v[134:137], v[82:97]
	v_mfma_f32_32x32x16_bf16 v[98:113], v[208:211], v[130:133], v[98:113]
	ds_read_b128 v[4:7], v243 offset:36992
	ds_read_b128 v[208:211], v243 offset:37120
	s_waitcnt lgkmcnt(0)
	v_mfma_f32_32x32x16_bf16 v[82:97], v[4:7], v[130:133], v[82:97]
	v_mfma_f32_32x32x16_bf16 v[98:113], v[12:15], v[126:129], v[98:113]
	v_mfma_f32_32x32x16_bf16 v[82:97], v[8:11], v[126:129], v[82:97]
	v_mfma_f32_32x32x16_bf16 v[98:113], v[196:199], v[122:125], v[98:113]
	v_mfma_f32_32x32x16_bf16 v[82:97], v[192:195], v[122:125], v[82:97]
	v_mfma_f32_32x32x16_bf16 v[98:113], v[204:207], v[118:121], v[98:113]
	v_mfma_f32_32x32x16_bf16 v[82:97], v[200:203], v[118:121], v[82:97]
	v_mfma_f32_32x32x16_bf16 v[98:113], v[212:215], v[114:117], v[98:113]
	v_mfma_f32_32x32x16_bf16 v[82:97], v[208:211], v[114:117], v[82:97]
	s_branch .Lmla_qkd
.Lmla_qk2:
	ds_read_b128 v[4:7], v240 offset:49152
	ds_read_b128 v[8:11], v240 offset:49280
	s_waitcnt lgkmcnt(0)
	v_mfma_f32_32x32x16_bf16 v[98:113], v[4:7], v[158:161], v[224:239]
	ds_read_b128 v[4:7], v240 offset:61440
	ds_read_b128 v[12:15], v240 offset:49408
	s_waitcnt lgkmcnt(0)
	v_mfma_f32_32x32x16_bf16 v[82:97], v[4:7], v[158:161], v[224:239]
	ds_read_b128 v[4:7], v241 offset:49152
	ds_read_b128 v[192:195], v241 offset:49280
	s_waitcnt lgkmcnt(0)
	v_mfma_f32_32x32x16_bf16 v[98:113], v[4:7], v[154:157], v[98:113]
	ds_read_b128 v[4:7], v241 offset:61440
	ds_read_b128 v[196:199], v241 offset:49408
	s_waitcnt lgkmcnt(0)
	v_mfma_f32_32x32x16_bf16 v[82:97], v[4:7], v[154:157], v[82:97]
	ds_read_b128 v[4:7], v242 offset:49152
	ds_read_b128 v[200:203], v242 offset:49280
	s_waitcnt lgkmcnt(0)
	v_mfma_f32_32x32x16_bf16 v[98:113], v[4:7], v[150:153], v[98:113]
	ds_read_b128 v[4:7], v242 offset:61440
	ds_read_b128 v[204:207], v242 offset:49408
	s_waitcnt lgkmcnt(0)
	v_mfma_f32_32x32x16_bf16 v[82:97], v[4:7], v[150:153], v[82:97]
	ds_read_b128 v[4:7], v243 offset:49152
	ds_read_b128 v[208:211], v243 offset:49280
	s_waitcnt lgkmcnt(0)
	v_mfma_f32_32x32x16_bf16 v[98:113], v[4:7], v[146:149], v[98:113]
	ds_read_b128 v[4:7], v243 offset:61440
	ds_read_b128 v[212:215], v243 offset:49408
	s_waitcnt lgkmcnt(0)
	v_mfma_f32_32x32x16_bf16 v[82:97], v[4:7], v[146:149], v[82:97]
	v_mfma_f32_32x32x16_bf16 v[98:113], v[8:11], v[142:145], v[98:113]
	ds_read_b128 v[4:7], v240 offset:61568
	ds_read_b128 v[8:11], v240 offset:61696
	s_waitcnt lgkmcnt(0)
	v_mfma_f32_32x32x16_bf16 v[82:97], v[4:7], v[142:145], v[82:97]
	v_mfma_f32_32x32x16_bf16 v[98:113], v[192:195], v[138:141], v[98:113]
	ds_read_b128 v[4:7], v241 offset:61568
	ds_read_b128 v[192:195], v241 offset:61696
	s_waitcnt lgkmcnt(0)
	v_mfma_f32_32x32x16_bf16 v[82:97], v[4:7], v[138:141], v[82:97]
	v_mfma_f32_32x32x16_bf16 v[98:113], v[200:203], v[134:137], v[98:113]
	ds_read_b128 v[4:7], v242 offset:61568
	ds_read_b128 v[200:203], v242 offset:61696
	s_waitcnt lgkmcnt(0)
	v_mfma_f32_32x32x16_bf16 v[82:97], v[4:7], v[134:137], v[82:97]
	v_mfma_f32_32x32x16_bf16 v[98:113], v[208:211], v[130:133], v[98:113]
	ds_read_b128 v[4:7], v243 offset:61568
	ds_read_b128 v[208:211], v243 offset:61696
	s_waitcnt lgkmcnt(0)
	v_mfma_f32_32x32x16_bf16 v[82:97], v[4:7], v[130:133], v[82:97]
	v_mfma_f32_32x32x16_bf16 v[98:113], v[12:15], v[126:129], v[98:113]
	v_mfma_f32_32x32x16_bf16 v[82:97], v[8:11], v[126:129], v[82:97]
	v_mfma_f32_32x32x16_bf16 v[98:113], v[196:199], v[122:125], v[98:113]
	v_mfma_f32_32x32x16_bf16 v[82:97], v[192:195], v[122:125], v[82:97]
	v_mfma_f32_32x32x16_bf16 v[98:113], v[204:207], v[118:121], v[98:113]
	v_mfma_f32_32x32x16_bf16 v[82:97], v[200:203], v[118:121], v[82:97]
	v_mfma_f32_32x32x16_bf16 v[98:113], v[212:215], v[114:117], v[98:113]
	v_mfma_f32_32x32x16_bf16 v[82:97], v[208:211], v[114:117], v[82:97]
;     DI NoBias bias(int) const { return NoBias(); }
;     DI WinBias bias(int q) const { const int j = tid_(q); WinBias B; B.base = j < 4 ? 100 : qpos - (k0base + 64 * (j - 4)) + 128; return B; }
; template <class BiasFn, bool PRE = false>
; DI void at_sm(f32x16& s0, f32x16& s1, f32x16 (&o)[4], float& m, float& l, const float c2, const BiasFn& bias, const int lane, bf16x8 (&pf)[4]) {
;     ...
;     int mi = (int)0x80000000;
; #pragma unroll
;     for (int i = 0; i < 16; ++i) {
;         const int key = (i & 3) + 8 * (i >> 2) + 4 * h;
;         if (!PRE) { s0[i] = fmaf(s0[i], c2, bias(key, nm)); s1[i] = fmaf(s1[i], c2, bias(32 + key, nm)); }
;         mi = max(mi, max((int)__float_as_uint(s0[i]), (int)__float_as_uint(s1[i])));
;     }
;     { const auto sw = __builtin_amdgcn_permlane32_swap((unsigned)mi, (unsigned)mi, false, false); mi = max((int)sw[0], (int)sw[1]); }
;     const float mx = __uint_as_float((unsigned)mi);
;     if (__any(mx > 8.0f)) {
;         const float d = fmaxf(mx, 0.f), alpha = __builtin_amdgcn_exp2f(-d);
;         m += d; l *= alpha;
; #pragma unroll
;         for (int t = 0; t < 4; ++t)
; #pragma unroll
;             for (int i = 0; i < 16; ++i) o[t][i] *= alpha;
; #pragma unroll
;         for (int i = 0; i < 16; ++i) { s0[i] -= d; s1[i] -= d; }
; template <int DQ, class Drv>
; DI void at_tile(const LAS unsigned char* ks, const LAS unsigned char* vs, const Drv& D, const int j, const AtRd& rd, const bf16x8 (&qf)[DQ / 16], f32x16 (&o)[4], float& m, float& l, const float c2, const int lane) {
;     ...
;         at_qk<DQ>(ks, rd, qf, a0, a1, Drv::PRE ? -m : 0.f);
.Lmla_qkd:
	s_nop 11
	v_max3_i32 v4, v82, v83, v84
	v_max3_i32 v5, v85, v86, v87
	v_max3_i32 v6, v88, v89, v90
	v_max3_i32 v7, v91, v92, v93
	v_max3_i32 v8, v94, v95, v96
	v_max3_i32 v9, v97, v98, v99
	v_max3_i32 v10, v100, v101, v102
	v_max3_i32 v11, v103, v104, v105
	v_max3_i32 v12, v106, v107, v108
	v_max3_i32 v13, v109, v110, v111
	v_max3_i32 v4, v4, v5, v6
	v_max3_i32 v5, v7, v8, v9
	v_max3_i32 v6, v10, v11, v12
	v_max3_i32 v7, v13, v112, v113
	v_max3_i32 v2, v4, v5, v6
	v_max_i32_e32 v2, v2, v7
	v_mov_b32_e32 v4, v2
	s_nop 1
	v_permlane32_swap_b32_e32 v2, v4
	v_max_i32_e32 v2, v2, v4
	v_cmp_lt_f32_e32 vcc, s58, v2
	s_cbranch_vccz .LBB0_555
	v_max_f32_e32 v2, v2, v2
	v_max_f32_e32 v4, 0, v2
	v_exp_f32_e64 v2, -v4
	v_add_f32_e32 v179, v179, v4
	v_xor_b32_e32 v224, 0x80000000, v179
	v_mov_b32_e32 v225, v224
	v_mov_b64_e32 v[226:227], v[224:225]
	v_mov_b64_e32 v[228:229], v[224:225]
	v_mov_b64_e32 v[230:231], v[224:225]
	v_mov_b64_e32 v[232:233], v[224:225]
	v_mov_b64_e32 v[234:235], v[224:225]
	v_mov_b64_e32 v[236:237], v[224:225]
	v_mov_b64_e32 v[238:239], v[224:225]
	v_sub_f32_e32 v113, v113, v4
	v_sub_f32_e32 v112, v112, v4
	v_mul_f32_e32 v173, v173, v2
	v_pk_mul_f32 v[80:81], v[80:81], v[2:3] op_sel_hi:[1,0]
	v_pk_mul_f32 v[78:79], v[78:79], v[2:3] op_sel_hi:[1,0]
	v_pk_mul_f32 v[76:77], v[76:77], v[2:3] op_sel_hi:[1,0]
	v_pk_mul_f32 v[74:75], v[74:75], v[2:3] op_sel_hi:[1,0]
	v_pk_mul_f32 v[72:73], v[72:73], v[2:3] op_sel_hi:[1,0]
	v_pk_mul_f32 v[70:71], v[70:71], v[2:3] op_sel_hi:[1,0]
	v_pk_mul_f32 v[68:69], v[68:69], v[2:3] op_sel_hi:[1,0]
	v_pk_mul_f32 v[66:67], v[66:67], v[2:3] op_sel_hi:[1,0]
	v_pk_mul_f32 v[64:65], v[64:65], v[2:3] op_sel_hi:[1,0]
	v_pk_mul_f32 v[62:63], v[62:63], v[2:3] op_sel_hi:[1,0]
	v_pk_mul_f32 v[60:61], v[60:61], v[2:3] op_sel_hi:[1,0]
	v_pk_mul_f32 v[58:59], v[58:59], v[2:3] op_sel_hi:[1,0]
	v_pk_mul_f32 v[56:57], v[56:57], v[2:3] op_sel_hi:[1,0]
	v_pk_mul_f32 v[54:55], v[54:55], v[2:3] op_sel_hi:[1,0]
	v_pk_mul_f32 v[52:53], v[52:53], v[2:3] op_sel_hi:[1,0]
	v_pk_mul_f32 v[50:51], v[50:51], v[2:3] op_sel_hi:[1,0]
	v_pk_mul_f32 v[48:49], v[48:49], v[2:3] op_sel_hi:[1,0]
	v_pk_mul_f32 v[46:47], v[46:47], v[2:3] op_sel_hi:[1,0]
	v_pk_mul_f32 v[44:45], v[44:45], v[2:3] op_sel_hi:[1,0]
	v_pk_mul_f32 v[42:43], v[42:43], v[2:3] op_sel_hi:[1,0]
	v_pk_mul_f32 v[40:41], v[40:41], v[2:3] op_sel_hi:[1,0]
	v_pk_mul_f32 v[38:39], v[38:39], v[2:3] op_sel_hi:[1,0]
	v_pk_mul_f32 v[36:37], v[36:37], v[2:3] op_sel_hi:[1,0]
	v_pk_mul_f32 v[34:35], v[34:35], v[2:3] op_sel_hi:[1,0]
	v_pk_mul_f32 v[32:33], v[32:33], v[2:3] op_sel_hi:[1,0]
	v_pk_mul_f32 v[30:31], v[30:31], v[2:3] op_sel_hi:[1,0]
	v_pk_mul_f32 v[28:29], v[28:29], v[2:3] op_sel_hi:[1,0]
	v_pk_mul_f32 v[26:27], v[26:27], v[2:3] op_sel_hi:[1,0]
	v_pk_mul_f32 v[24:25], v[24:25], v[2:3] op_sel_hi:[1,0]
	v_pk_mul_f32 v[22:23], v[22:23], v[2:3] op_sel_hi:[1,0]
	v_pk_mul_f32 v[20:21], v[20:21], v[2:3] op_sel_hi:[1,0]
	v_pk_mul_f32 v[18:19], v[18:19], v[2:3] op_sel_hi:[1,0]
	v_sub_f32_e32 v111, v111, v4
	v_sub_f32_e32 v110, v110, v4
	v_sub_f32_e32 v109, v109, v4
	v_sub_f32_e32 v108, v108, v4
	v_sub_f32_e32 v107, v107, v4
	v_sub_f32_e32 v106, v106, v4
	v_sub_f32_e32 v105, v105, v4
	v_sub_f32_e32 v104, v104, v4
	v_sub_f32_e32 v103, v103, v4
	v_sub_f32_e32 v102, v102, v4
	v_sub_f32_e32 v101, v101, v4
	v_sub_f32_e32 v100, v100, v4
	v_sub_f32_e32 v99, v99, v4
	v_sub_f32_e32 v98, v98, v4
	v_sub_f32_e32 v97, v97, v4
	v_sub_f32_e32 v96, v96, v4
	v_sub_f32_e32 v95, v95, v4
	v_sub_f32_e32 v94, v94, v4
	v_sub_f32_e32 v93, v93, v4
	v_sub_f32_e32 v92, v92, v4
	v_sub_f32_e32 v91, v91, v4
	v_sub_f32_e32 v90, v90, v4
	v_sub_f32_e32 v89, v89, v4
	v_sub_f32_e32 v88, v88, v4
	v_sub_f32_e32 v87, v87, v4
	v_sub_f32_e32 v86, v86, v4
	v_sub_f32_e32 v85, v85, v4
	v_sub_f32_e32 v84, v84, v4
	v_sub_f32_e32 v83, v83, v4
	v_sub_f32_e32 v82, v82, v4
	s_branch .LBB0_555
